# v78 with the barrier poll back-off raised from s_sleep 1 to s_sleep 6 (fewer polls on the arrival-counter line)
# speedup vs baseline: 1.0032x; 1.0032x over previous
; __device__ __forceinline__ unsigned xb_ld(unsigned* p)              { return __hip_atomic_load(p, __ATOMIC_RELAXED, __HIP_MEMORY_SCOPE_AGENT); }
; __device__ __forceinline__ void xcd_barrier_complete(unsigned* bar, unsigned x, unsigned& nloc, unsigned& nx, unsigned& bal) {
;     const unsigned G = gridDim.x * gridDim.y * gridDim.z;
;     unsigned sum, cnt, mine, even, sp = 0u;
;     for (;;) {
;         sum = 0u; cnt = 0u; mine = 0u; even = 1u;
; #pragma unroll
;         for (unsigned j = 0; j < 16; ++j) { const unsigned c = xb_ld(&bar[XB_XCNT(j)]); sum += c; cnt += (c > 0u) ? 1u : 0u; mine = (j == x) ? c : mine; even &= (c == (j < 8u ? G / 8u : 0u)) ? 1u : 0u; }
;         if (sum == G) break;
;         __builtin_amdgcn_s_sleep(1);
;         if ((++sp & 255u) == 0u) { if (xb_ld(&bar[XB_TMO])) break; if (sp > XB_SPIN_CAP) { atomicAdd(&bar[XB_TMO], 1u); break; } }
;     }
.LBB0_67:
	global_load_dword v9, v8, s[28:29] offset:1024 sc1
	global_load_dword v10, v8, s[28:29] offset:1280 sc1
	global_load_dword v11, v8, s[28:29] offset:1536 sc1
	global_load_dword v12, v8, s[28:29] offset:1792 sc1
	global_load_dword v13, v8, s[28:29] offset:2048 sc1
	global_load_dword v14, v8, s[28:29] offset:2304 sc1
	global_load_dword v15, v8, s[28:29] offset:2560 sc1
	global_load_dword v16, v8, s[28:29] offset:2816 sc1
	global_load_dword v0, v8, s[28:29] offset:3072 sc1
	global_load_dword v1, v8, s[28:29] offset:3328 sc1
	global_load_dword v2, v8, s[28:29] offset:3584 sc1
	global_load_dword v3, v8, s[28:29] offset:3840 sc1
	global_load_dword v4, v8, s[4:5] sc1
	global_load_dword v5, v8, s[6:7] sc1
	global_load_dword v6, v8, s[12:13] sc1
	global_load_dword v7, v8, s[14:15] sc1
	s_waitcnt vmcnt(15)
	v_readfirstlane_b32 s34, v9
	s_waitcnt vmcnt(14)
	v_add_u32_e32 v9, v10, v9
	s_waitcnt vmcnt(13)
	v_add_u32_e32 v9, v9, v11
	s_waitcnt vmcnt(12)
	v_add_u32_e32 v9, v9, v12
	s_waitcnt vmcnt(11)
	v_add_u32_e32 v9, v9, v13
	s_waitcnt vmcnt(10)
	v_add_u32_e32 v9, v9, v14
	s_waitcnt vmcnt(9)
	v_add_u32_e32 v9, v9, v15
	s_waitcnt vmcnt(8)
	v_add_u32_e32 v9, v9, v16
	s_waitcnt vmcnt(7)
	v_add_u32_e32 v9, v9, v0
	s_waitcnt vmcnt(6)
	v_add_u32_e32 v9, v9, v1
	s_waitcnt vmcnt(5)
	v_add_u32_e32 v9, v9, v2
	s_waitcnt vmcnt(4)
	v_add_u32_e32 v9, v9, v3
	s_waitcnt vmcnt(3)
	v_add_u32_e32 v9, v9, v4
	s_waitcnt vmcnt(2)
	v_add_u32_e32 v9, v9, v5
	s_waitcnt vmcnt(1)
	v_add_u32_e32 v9, v9, v6
	s_waitcnt vmcnt(0)
	v_add_u32_e32 v9, v9, v7
	v_cmp_eq_u32_e32 vcc, s3, v9
	v_readfirstlane_b32 s27, v10
	v_readfirstlane_b32 s30, v11
	v_readfirstlane_b32 s26, v12
	v_readfirstlane_b32 s25, v13
	v_readfirstlane_b32 s24, v14
	v_readfirstlane_b32 s31, v15
	v_readfirstlane_b32 s35, v16
	s_cbranch_vccnz .LBB0_65
	s_and_b32 s18, s36, 0xff
	s_mov_b64 s[20:21], -1
	s_mov_b64 s[16:17], 0
	s_cmp_eq_u32 s18, 0
	s_mov_b64 s[18:19], -1
	s_mov_b64 s[22:23], -1
	s_sleep 6
	s_cbranch_scc0 .LBB0_70
	global_load_dword v9, v8, s[28:29] offset:512 sc1
	s_mov_b64 s[18:19], 0
	s_mov_b64 s[16:17], -1
	s_mov_b64 s[22:23], 0
	s_waitcnt vmcnt(0)
	v_cmp_eq_u32_e32 vcc, 0, v9
	s_cbranch_vccnz .LBB0_72

; __device__ __forceinline__ unsigned xb_ld(unsigned* p)              { return __hip_atomic_load(p, __ATOMIC_RELAXED, __HIP_MEMORY_SCOPE_AGENT); }
; __device__ __forceinline__ unsigned xb_add(unsigned* p, unsigned v) { return __hip_atomic_fetch_add(p, v, __ATOMIC_RELAXED, __HIP_MEMORY_SCOPE_AGENT); }
; #define XB_SPIN(cond, bar) do { unsigned _sp = 0; while (cond) { __builtin_amdgcn_s_sleep(1); \
;     if ((++_sp & 255u) == 0u) { if (xb_ld(&(bar)[XB_TMO])) break; if (_sp > XB_SPIN_CAP) { atomicAdd(&(bar)[XB_TMO], 1u); break; } } } } while (0)
; __device__ __forceinline__ void xcd_barrier(const XcdBarrier& b, const bool xb_leader) {
;     ...
;             const unsigned og = xb_add(&bar[XB_TOP], 1u);
;             const unsigned tg = og / nx;
;             if (og + 1u == (tg + 1u) * nx) xb_add(&bar[XB_TOPGEN], 1u);
;             else XB_SPIN(xb_ld(&bar[XB_TOPGEN]) == tg, bar);
.LBB0_91:
	s_and_b32 s22, s3, 0xff
	s_mov_b64 s[20:21], -1
	s_cmp_lg_u32 s22, 0
	s_mov_b64 s[24:25], -1
	s_sleep 6
	s_cbranch_scc1 .LBB0_94
	global_load_dword v2, v1, s[28:29] offset:512 sc1
	s_waitcnt vmcnt(0)
	v_cmp_eq_u32_e32 vcc, 0, v2
	s_cbranch_vccnz .LBB0_96
	s_mov_b64 s[24:25], 0
	s_mov_b64 s[22:23], -1

; __device__ __forceinline__ unsigned xb_ld(unsigned* p)              { return __hip_atomic_load(p, __ATOMIC_RELAXED, __HIP_MEMORY_SCOPE_AGENT); }
; #define XB_SPIN(cond, bar) do { unsigned _sp = 0; while (cond) { __builtin_amdgcn_s_sleep(1); \
;     if ((++_sp & 255u) == 0u) { if (xb_ld(&(bar)[XB_TMO])) break; if (_sp > XB_SPIN_CAP) { atomicAdd(&(bar)[XB_TMO], 1u); break; } } } } while (0)
; __device__ __forceinline__ void xcd_barrier(const XcdBarrier& b, const bool xb_leader) {
;     ...
;         } else {
;             XB_SPIN(xb_ld(&bar[XB_XGEN(b.x)]) == gen, bar);
;             __builtin_amdgcn_fence(__ATOMIC_ACQUIRE, "agent");
.LBB0_108:
	s_and_b32 s22, s3, 0xff
	s_cmp_lg_u32 s22, 0
	s_mov_b64 s[24:25], -1
	s_sleep 6
	s_cbranch_scc1 .LBB0_111
	global_load_dword v1, v0, s[14:15] sc1
	s_waitcnt vmcnt(0)
	v_cmp_eq_u32_e32 vcc, 0, v1
	s_cbranch_vccnz .LBB0_113
	s_mov_b64 s[24:25], 0
	s_mov_b64 s[22:23], -1

; __device__ __forceinline__ unsigned xb_ld(unsigned* p)              { return __hip_atomic_load(p, __ATOMIC_RELAXED, __HIP_MEMORY_SCOPE_AGENT); }
; __device__ __forceinline__ unsigned xb_add(unsigned* p, unsigned v) { return __hip_atomic_fetch_add(p, v, __ATOMIC_RELAXED, __HIP_MEMORY_SCOPE_AGENT); }
; #define XB_SPIN(cond, bar) do { unsigned _sp = 0; while (cond) { __builtin_amdgcn_s_sleep(1); \
;     if ((++_sp & 255u) == 0u) { if (xb_ld(&(bar)[XB_TMO])) break; if (_sp > XB_SPIN_CAP) { atomicAdd(&(bar)[XB_TMO], 1u); break; } } } } while (0)
; __device__ __forceinline__ void xcc_barrier(unsigned* bar, unsigned* cnt, unsigned nloc, const bool xb_leader) {
;     ...
;     if (xb_leader) {
;         __builtin_amdgcn_s_waitcnt(0);
;         const unsigned old = xb_add(cnt, 1u), target = (old / nloc + 1u) * nloc;
;         XB_SPIN(xb_ld(cnt) < target, bar);
.LBB0_140:
	s_and_b32 s16, s3, 0xff
	s_mov_b64 s[14:15], -1
	s_cmp_lg_u32 s16, 0
	s_mov_b64 s[18:19], -1
	s_sleep 6
	s_cbranch_scc1 .LBB0_143
	global_load_dword v2, v0, s[28:29] offset:512 sc1
	s_waitcnt vmcnt(0)
	v_cmp_eq_u32_e32 vcc, 0, v2
	s_cbranch_vccnz .LBB0_145
	s_mov_b64 s[18:19], 0
	s_mov_b64 s[16:17], -1

; __device__ __forceinline__ unsigned xb_ld(unsigned* p)              { return __hip_atomic_load(p, __ATOMIC_RELAXED, __HIP_MEMORY_SCOPE_AGENT); }
; __device__ __forceinline__ void xcd_barrier_complete(unsigned* bar, unsigned x, unsigned& nloc, unsigned& nx, unsigned& bal) {
;     ...
;     for (;;) {
;         sum = 0u; cnt = 0u; mine = 0u; even = 1u;
; #pragma unroll
;         for (unsigned j = 0; j < 16; ++j) { const unsigned c = xb_ld(&bar[XB_XCNT(j)]); sum += c; cnt += (c > 0u) ? 1u : 0u; mine = (j == x) ? c : mine; even &= (c == (j < 8u ? G / 8u : 0u)) ? 1u : 0u; }
;         if (sum == G) break;
;         __builtin_amdgcn_s_sleep(1);
;         if ((++sp & 255u) == 0u) { if (xb_ld(&bar[XB_TMO])) break; if (sp > XB_SPIN_CAP) { atomicAdd(&bar[XB_TMO], 1u); break; } }
;     }
.LBB0_159:
	global_load_dword v9, v8, s[28:29] offset:1024 sc1
	global_load_dword v10, v8, s[28:29] offset:1280 sc1
	global_load_dword v11, v8, s[28:29] offset:1536 sc1
	global_load_dword v12, v8, s[28:29] offset:1792 sc1
	global_load_dword v13, v8, s[28:29] offset:2048 sc1
	global_load_dword v14, v8, s[28:29] offset:2304 sc1
	global_load_dword v15, v8, s[28:29] offset:2560 sc1
	global_load_dword v16, v8, s[28:29] offset:2816 sc1
	global_load_dword v0, v8, s[28:29] offset:3072 sc1
	global_load_dword v1, v8, s[28:29] offset:3328 sc1
	global_load_dword v2, v8, s[28:29] offset:3584 sc1
	global_load_dword v3, v8, s[28:29] offset:3840 sc1
	global_load_dword v4, v8, s[6:7] sc1
	global_load_dword v5, v8, s[8:9] sc1
	global_load_dword v6, v8, s[10:11] sc1
	global_load_dword v7, v8, s[12:13] sc1
	s_waitcnt vmcnt(15)
	v_readfirstlane_b32 s30, v9
	s_waitcnt vmcnt(14)
	v_add_u32_e32 v9, v10, v9
	s_waitcnt vmcnt(13)
	v_add_u32_e32 v9, v9, v11
	s_waitcnt vmcnt(12)
	v_add_u32_e32 v9, v9, v12
	s_waitcnt vmcnt(11)
	v_add_u32_e32 v9, v9, v13
	s_waitcnt vmcnt(10)
	v_add_u32_e32 v9, v9, v14
	s_waitcnt vmcnt(9)
	v_add_u32_e32 v9, v9, v15
	s_waitcnt vmcnt(8)
	v_add_u32_e32 v9, v9, v16
	s_waitcnt vmcnt(7)
	v_add_u32_e32 v9, v9, v0
	s_waitcnt vmcnt(6)
	v_add_u32_e32 v9, v9, v1
	s_waitcnt vmcnt(5)
	v_add_u32_e32 v9, v9, v2
	s_waitcnt vmcnt(4)
	v_add_u32_e32 v9, v9, v3
	s_waitcnt vmcnt(3)
	v_add_u32_e32 v9, v9, v4
	s_waitcnt vmcnt(2)
	v_add_u32_e32 v9, v9, v5
	s_waitcnt vmcnt(1)
	v_add_u32_e32 v9, v9, v6
	s_waitcnt vmcnt(0)
	v_add_u32_e32 v9, v9, v7
	v_cmp_eq_u32_e32 vcc, s3, v9
	v_readfirstlane_b32 s25, v10
	v_readfirstlane_b32 s26, v11
	v_readfirstlane_b32 s24, v12
	v_readfirstlane_b32 s23, v13
	v_readfirstlane_b32 s22, v14
	v_readfirstlane_b32 s27, v15
	v_readfirstlane_b32 s31, v16
	s_cbranch_vccnz .LBB0_157
	s_and_b32 s16, s36, 0xff
	s_mov_b64 s[18:19], -1
	s_mov_b64 s[14:15], 0
	s_cmp_eq_u32 s16, 0
	s_mov_b64 s[16:17], -1
	s_mov_b64 s[20:21], -1
	s_sleep 6
	s_cbranch_scc0 .LBB0_163
	global_load_dword v9, v8, s[28:29] offset:512 sc1
	s_mov_b64 s[16:17], 0
	s_mov_b64 s[14:15], -1
	s_mov_b64 s[20:21], 0
	s_waitcnt vmcnt(0)
	v_cmp_eq_u32_e32 vcc, 0, v9
	s_cbranch_vccz .LBB0_163
	s_cmp_lt_u32 s36, 0x40001
	s_mov_b64 s[14:15], 0
	s_cselect_b64 s[20:21], -1, 0

; __device__ __forceinline__ unsigned xb_ld(unsigned* p)              { return __hip_atomic_load(p, __ATOMIC_RELAXED, __HIP_MEMORY_SCOPE_AGENT); }
; __device__ __forceinline__ unsigned xb_add(unsigned* p, unsigned v) { return __hip_atomic_fetch_add(p, v, __ATOMIC_RELAXED, __HIP_MEMORY_SCOPE_AGENT); }
; #define XB_SPIN(cond, bar) do { unsigned _sp = 0; while (cond) { __builtin_amdgcn_s_sleep(1); \
;     if ((++_sp & 255u) == 0u) { if (xb_ld(&(bar)[XB_TMO])) break; if (_sp > XB_SPIN_CAP) { atomicAdd(&(bar)[XB_TMO], 1u); break; } } } } while (0)
; __device__ __forceinline__ void xcd_barrier(const XcdBarrier& b, const bool xb_leader) {
;     ...
;             const unsigned og = xb_add(&bar[XB_TOP], 1u);
;             const unsigned tg = og / nx;
;             if (og + 1u == (tg + 1u) * nx) xb_add(&bar[XB_TOPGEN], 1u);
;             else XB_SPIN(xb_ld(&bar[XB_TOPGEN]) == tg, bar);
.LBB0_184:
	s_and_b32 s20, s3, 0xff
	s_mov_b64 s[18:19], -1
	s_cmp_lg_u32 s20, 0
	s_mov_b64 s[22:23], -1
	s_sleep 6
	s_cbranch_scc1 .LBB0_187
	global_load_dword v2, v1, s[28:29] offset:512 sc1
	s_waitcnt vmcnt(0)
	v_cmp_eq_u32_e32 vcc, 0, v2
	s_cbranch_vccnz .LBB0_189
	s_mov_b64 s[22:23], 0
	s_mov_b64 s[20:21], -1

; __device__ __forceinline__ unsigned xb_ld(unsigned* p)              { return __hip_atomic_load(p, __ATOMIC_RELAXED, __HIP_MEMORY_SCOPE_AGENT); }
; #define XB_SPIN(cond, bar) do { unsigned _sp = 0; while (cond) { __builtin_amdgcn_s_sleep(1); \
;     if ((++_sp & 255u) == 0u) { if (xb_ld(&(bar)[XB_TMO])) break; if (_sp > XB_SPIN_CAP) { atomicAdd(&(bar)[XB_TMO], 1u); break; } } } } while (0)
; __device__ __forceinline__ void xcd_barrier(const XcdBarrier& b, const bool xb_leader) {
;     ...
;         } else {
;             XB_SPIN(xb_ld(&bar[XB_XGEN(b.x)]) == gen, bar);
;             __builtin_amdgcn_fence(__ATOMIC_ACQUIRE, "agent");
.LBB0_201:
	s_and_b32 s20, s3, 0xff
	s_cmp_lg_u32 s20, 0
	s_mov_b64 s[22:23], -1
	s_sleep 6
	s_cbranch_scc1 .LBB0_204
	global_load_dword v1, v0, s[12:13] sc1
	s_waitcnt vmcnt(0)
	v_cmp_eq_u32_e32 vcc, 0, v1
	s_cbranch_vccnz .LBB0_206
	s_mov_b64 s[22:23], 0
	s_mov_b64 s[20:21], -1

; __device__ __forceinline__ unsigned xb_ld(unsigned* p)              { return __hip_atomic_load(p, __ATOMIC_RELAXED, __HIP_MEMORY_SCOPE_AGENT); }
; __device__ __forceinline__ void xcd_barrier_complete(unsigned* bar, unsigned x, unsigned& nloc, unsigned& nx, unsigned& bal) {
;     ...
;     for (;;) {
;         sum = 0u; cnt = 0u; mine = 0u; even = 1u;
; #pragma unroll
;         for (unsigned j = 0; j < 16; ++j) { const unsigned c = xb_ld(&bar[XB_XCNT(j)]); sum += c; cnt += (c > 0u) ? 1u : 0u; mine = (j == x) ? c : mine; even &= (c == (j < 8u ? G / 8u : 0u)) ? 1u : 0u; }
;         if (sum == G) break;
;         __builtin_amdgcn_s_sleep(1);
;         if ((++sp & 255u) == 0u) { if (xb_ld(&bar[XB_TMO])) break; if (sp > XB_SPIN_CAP) { atomicAdd(&bar[XB_TMO], 1u); break; } }
;     }
.LBB0_316:
	global_load_dword v9, v8, s[28:29] offset:1024 sc1
	global_load_dword v10, v8, s[28:29] offset:1280 sc1
	global_load_dword v11, v8, s[28:29] offset:1536 sc1
	global_load_dword v12, v8, s[28:29] offset:1792 sc1
	global_load_dword v13, v8, s[28:29] offset:2048 sc1
	global_load_dword v14, v8, s[28:29] offset:2304 sc1
	global_load_dword v15, v8, s[28:29] offset:2560 sc1
	global_load_dword v16, v8, s[28:29] offset:2816 sc1
	global_load_dword v0, v8, s[28:29] offset:3072 sc1
	global_load_dword v1, v8, s[28:29] offset:3328 sc1
	global_load_dword v2, v8, s[28:29] offset:3584 sc1
	global_load_dword v3, v8, s[28:29] offset:3840 sc1
	global_load_dword v4, v8, s[6:7] sc1
	global_load_dword v5, v8, s[8:9] sc1
	global_load_dword v6, v8, s[10:11] sc1
	global_load_dword v7, v8, s[12:13] sc1
	s_waitcnt vmcnt(15)
	v_readfirstlane_b32 s30, v9
	s_waitcnt vmcnt(14)
	v_add_u32_e32 v9, v10, v9
	s_waitcnt vmcnt(13)
	v_add_u32_e32 v9, v9, v11
	s_waitcnt vmcnt(12)
	v_add_u32_e32 v9, v9, v12
	s_waitcnt vmcnt(11)
	v_add_u32_e32 v9, v9, v13
	s_waitcnt vmcnt(10)
	v_add_u32_e32 v9, v9, v14
	s_waitcnt vmcnt(9)
	v_add_u32_e32 v9, v9, v15
	s_waitcnt vmcnt(8)
	v_add_u32_e32 v9, v9, v16
	s_waitcnt vmcnt(7)
	v_add_u32_e32 v9, v9, v0
	s_waitcnt vmcnt(6)
	v_add_u32_e32 v9, v9, v1
	s_waitcnt vmcnt(5)
	v_add_u32_e32 v9, v9, v2
	s_waitcnt vmcnt(4)
	v_add_u32_e32 v9, v9, v3
	s_waitcnt vmcnt(3)
	v_add_u32_e32 v9, v9, v4
	s_waitcnt vmcnt(2)
	v_add_u32_e32 v9, v9, v5
	s_waitcnt vmcnt(1)
	v_add_u32_e32 v9, v9, v6
	s_waitcnt vmcnt(0)
	v_add_u32_e32 v9, v9, v7
	v_cmp_eq_u32_e32 vcc, s3, v9
	v_readfirstlane_b32 s25, v10
	v_readfirstlane_b32 s26, v11
	v_readfirstlane_b32 s24, v12
	v_readfirstlane_b32 s23, v13
	v_readfirstlane_b32 s22, v14
	v_readfirstlane_b32 s27, v15
	v_readfirstlane_b32 s31, v16
	s_cbranch_vccnz .LBB0_314
	s_and_b32 s16, s36, 0xff
	s_mov_b64 s[18:19], -1
	s_mov_b64 s[14:15], 0
	s_cmp_eq_u32 s16, 0
	s_mov_b64 s[16:17], -1
	s_mov_b64 s[20:21], -1
	s_sleep 6
	s_cbranch_scc0 .LBB0_319
	global_load_dword v9, v8, s[28:29] offset:512 sc1
	s_mov_b64 s[16:17], 0
	s_mov_b64 s[14:15], -1
	s_mov_b64 s[20:21], 0
	s_waitcnt vmcnt(0)
	v_cmp_eq_u32_e32 vcc, 0, v9
	s_cbranch_vccnz .LBB0_321

; __device__ __forceinline__ unsigned xb_ld(unsigned* p)              { return __hip_atomic_load(p, __ATOMIC_RELAXED, __HIP_MEMORY_SCOPE_AGENT); }
; __device__ __forceinline__ unsigned xb_add(unsigned* p, unsigned v) { return __hip_atomic_fetch_add(p, v, __ATOMIC_RELAXED, __HIP_MEMORY_SCOPE_AGENT); }
; #define XB_SPIN(cond, bar) do { unsigned _sp = 0; while (cond) { __builtin_amdgcn_s_sleep(1); \
;     if ((++_sp & 255u) == 0u) { if (xb_ld(&(bar)[XB_TMO])) break; if (_sp > XB_SPIN_CAP) { atomicAdd(&(bar)[XB_TMO], 1u); break; } } } } while (0)
; __device__ __forceinline__ void xcc_barrier(unsigned* bar, unsigned* cnt, unsigned nloc, const bool xb_leader) {
;     ...
;     if (xb_leader) {
;         __builtin_amdgcn_s_waitcnt(0);
;         const unsigned old = xb_add(cnt, 1u), target = (old / nloc + 1u) * nloc;
;         XB_SPIN(xb_ld(cnt) < target, bar);
.LBB0_751:
	s_and_b32 s14, s3, 0xff
	s_mov_b64 s[12:13], -1
	s_cmp_lg_u32 s14, 0
	s_mov_b64 s[16:17], -1
	s_sleep 6
	s_cbranch_scc1 .LBB0_754
	global_load_dword v2, v0, s[28:29] offset:512 sc1
	s_waitcnt vmcnt(0)
	v_cmp_eq_u32_e32 vcc, 0, v2
	s_cbranch_vccnz .LBB0_756
	s_mov_b64 s[16:17], 0
	s_mov_b64 s[14:15], -1

; __device__ __forceinline__ unsigned xb_ld(unsigned* p)              { return __hip_atomic_load(p, __ATOMIC_RELAXED, __HIP_MEMORY_SCOPE_AGENT); }
; __device__ __forceinline__ void xcd_barrier_complete(unsigned* bar, unsigned x, unsigned& nloc, unsigned& nx, unsigned& bal) {
;     ...
;     for (;;) {
;         sum = 0u; cnt = 0u; mine = 0u; even = 1u;
; #pragma unroll
;         for (unsigned j = 0; j < 16; ++j) { const unsigned c = xb_ld(&bar[XB_XCNT(j)]); sum += c; cnt += (c > 0u) ? 1u : 0u; mine = (j == x) ? c : mine; even &= (c == (j < 8u ? G / 8u : 0u)) ? 1u : 0u; }
;         if (sum == G) break;
;         __builtin_amdgcn_s_sleep(1);
;         if ((++sp & 255u) == 0u) { if (xb_ld(&bar[XB_TMO])) break; if (sp > XB_SPIN_CAP) { atomicAdd(&bar[XB_TMO], 1u); break; } }
;     }
.LBB0_800:
	global_load_dword v9, v8, s[28:29] offset:1024 sc1
	global_load_dword v10, v8, s[28:29] offset:1280 sc1
	global_load_dword v11, v8, s[28:29] offset:1536 sc1
	global_load_dword v12, v8, s[28:29] offset:1792 sc1
	global_load_dword v13, v8, s[28:29] offset:2048 sc1
	global_load_dword v14, v8, s[28:29] offset:2304 sc1
	global_load_dword v15, v8, s[28:29] offset:2560 sc1
	global_load_dword v16, v8, s[28:29] offset:2816 sc1
	global_load_dword v0, v8, s[28:29] offset:3072 sc1
	global_load_dword v1, v8, s[28:29] offset:3328 sc1
	global_load_dword v2, v8, s[28:29] offset:3584 sc1
	global_load_dword v3, v8, s[28:29] offset:3840 sc1
	global_load_dword v4, v8, s[4:5] sc1
	global_load_dword v5, v8, s[6:7] sc1
	global_load_dword v6, v8, s[8:9] sc1
	global_load_dword v7, v8, s[10:11] sc1
	s_waitcnt vmcnt(15)
	v_readfirstlane_b32 s30, v9
	s_waitcnt vmcnt(14)
	v_add_u32_e32 v9, v10, v9
	s_waitcnt vmcnt(13)
	v_add_u32_e32 v9, v9, v11
	s_waitcnt vmcnt(12)
	v_add_u32_e32 v9, v9, v12
	s_waitcnt vmcnt(11)
	v_add_u32_e32 v9, v9, v13
	s_waitcnt vmcnt(10)
	v_add_u32_e32 v9, v9, v14
	s_waitcnt vmcnt(9)
	v_add_u32_e32 v9, v9, v15
	s_waitcnt vmcnt(8)
	v_add_u32_e32 v9, v9, v16
	s_waitcnt vmcnt(7)
	v_add_u32_e32 v9, v9, v0
	s_waitcnt vmcnt(6)
	v_add_u32_e32 v9, v9, v1
	s_waitcnt vmcnt(5)
	v_add_u32_e32 v9, v9, v2
	s_waitcnt vmcnt(4)
	v_add_u32_e32 v9, v9, v3
	s_waitcnt vmcnt(3)
	v_add_u32_e32 v9, v9, v4
	s_waitcnt vmcnt(2)
	v_add_u32_e32 v9, v9, v5
	s_waitcnt vmcnt(1)
	v_add_u32_e32 v9, v9, v6
	s_waitcnt vmcnt(0)
	v_add_u32_e32 v9, v9, v7
	v_cmp_eq_u32_e32 vcc, s3, v9
	v_readfirstlane_b32 s25, v10
	v_readfirstlane_b32 s26, v11
	v_readfirstlane_b32 s24, v12
	v_readfirstlane_b32 s23, v13
	v_readfirstlane_b32 s22, v14
	v_readfirstlane_b32 s27, v15
	v_readfirstlane_b32 s31, v16
	s_cbranch_vccnz .LBB0_798
	s_and_b32 s14, s36, 0xff
	s_mov_b64 s[16:17], -1
	s_mov_b64 s[12:13], 0
	s_cmp_eq_u32 s14, 0
	s_mov_b64 s[14:15], -1
	s_mov_b64 s[20:21], -1
	s_sleep 6
	s_cbranch_scc0 .LBB0_804
	global_load_dword v9, v8, s[28:29] offset:512 sc1
	s_mov_b64 s[14:15], 0
	s_mov_b64 s[12:13], -1
	s_mov_b64 s[20:21], 0
	s_waitcnt vmcnt(0)
	v_cmp_eq_u32_e32 vcc, 0, v9
	s_cbranch_vccz .LBB0_804
	s_cmp_lt_u32 s36, 0x40001
	s_mov_b64 s[12:13], 0
	s_cselect_b64 s[20:21], -1, 0

; __device__ __forceinline__ unsigned xb_ld(unsigned* p)              { return __hip_atomic_load(p, __ATOMIC_RELAXED, __HIP_MEMORY_SCOPE_AGENT); }
; __device__ __forceinline__ unsigned xb_add(unsigned* p, unsigned v) { return __hip_atomic_fetch_add(p, v, __ATOMIC_RELAXED, __HIP_MEMORY_SCOPE_AGENT); }
; #define XB_SPIN(cond, bar) do { unsigned _sp = 0; while (cond) { __builtin_amdgcn_s_sleep(1); \
;     if ((++_sp & 255u) == 0u) { if (xb_ld(&(bar)[XB_TMO])) break; if (_sp > XB_SPIN_CAP) { atomicAdd(&(bar)[XB_TMO], 1u); break; } } } } while (0)
; __device__ __forceinline__ void xcd_barrier(const XcdBarrier& b, const bool xb_leader) {
;     ...
;             const unsigned og = xb_add(&bar[XB_TOP], 1u);
;             const unsigned tg = og / nx;
;             if (og + 1u == (tg + 1u) * nx) xb_add(&bar[XB_TOPGEN], 1u);
;             else XB_SPIN(xb_ld(&bar[XB_TOPGEN]) == tg, bar);
.LBB0_825:
	s_and_b32 s20, s3, 0xff
	s_mov_b64 s[16:17], -1
	s_cmp_lg_u32 s20, 0
	s_mov_b64 s[22:23], -1
	s_sleep 6
	s_cbranch_scc1 .LBB0_828
	global_load_dword v2, v1, s[28:29] offset:512 sc1
	s_waitcnt vmcnt(0)
	v_cmp_eq_u32_e32 vcc, 0, v2
	s_cbranch_vccnz .LBB0_830
	s_mov_b64 s[22:23], 0
	s_mov_b64 s[20:21], -1

; __device__ __forceinline__ unsigned xb_ld(unsigned* p)              { return __hip_atomic_load(p, __ATOMIC_RELAXED, __HIP_MEMORY_SCOPE_AGENT); }
; #define XB_SPIN(cond, bar) do { unsigned _sp = 0; while (cond) { __builtin_amdgcn_s_sleep(1); \
;     if ((++_sp & 255u) == 0u) { if (xb_ld(&(bar)[XB_TMO])) break; if (_sp > XB_SPIN_CAP) { atomicAdd(&(bar)[XB_TMO], 1u); break; } } } } while (0)
; __device__ __forceinline__ void xcd_barrier(const XcdBarrier& b, const bool xb_leader) {
;     ...
;         } else {
;             XB_SPIN(xb_ld(&bar[XB_XGEN(b.x)]) == gen, bar);
;             __builtin_amdgcn_fence(__ATOMIC_ACQUIRE, "agent");
.LBB0_842:
	s_and_b32 s20, s3, 0xff
	s_cmp_lg_u32 s20, 0
	s_mov_b64 s[22:23], -1
	s_sleep 6
	s_cbranch_scc1 .LBB0_845
	global_load_dword v1, v0, s[10:11] sc1
	s_waitcnt vmcnt(0)
	v_cmp_eq_u32_e32 vcc, 0, v1
	s_cbranch_vccnz .LBB0_847
	s_mov_b64 s[22:23], 0
	s_mov_b64 s[20:21], -1

; __device__ __forceinline__ unsigned xb_ld(unsigned* p)              { return __hip_atomic_load(p, __ATOMIC_RELAXED, __HIP_MEMORY_SCOPE_AGENT); }
; __device__ __forceinline__ unsigned xb_add(unsigned* p, unsigned v) { return __hip_atomic_fetch_add(p, v, __ATOMIC_RELAXED, __HIP_MEMORY_SCOPE_AGENT); }
; #define XB_SPIN(cond, bar) do { unsigned _sp = 0; while (cond) { __builtin_amdgcn_s_sleep(1); \
;     if ((++_sp & 255u) == 0u) { if (xb_ld(&(bar)[XB_TMO])) break; if (_sp > XB_SPIN_CAP) { atomicAdd(&(bar)[XB_TMO], 1u); break; } } } } while (0)
; __device__ __forceinline__ void xcc_barrier(unsigned* bar, unsigned* cnt, unsigned nloc, const bool xb_leader) {
;     ...
;     if (xb_leader) {
;         __builtin_amdgcn_s_waitcnt(0);
;         const unsigned old = xb_add(cnt, 1u), target = (old / nloc + 1u) * nloc;
;         XB_SPIN(xb_ld(cnt) < target, bar);
.LBB0_884:
	s_and_b32 s16, s3, 0xff
	s_mov_b64 s[14:15], -1
	s_cmp_lg_u32 s16, 0
	s_mov_b64 s[22:23], -1
	s_sleep 6
	s_cbranch_scc1 .LBB0_887
	global_load_dword v2, v0, s[28:29] offset:512 sc1
	s_waitcnt vmcnt(0)
	v_cmp_eq_u32_e32 vcc, 0, v2
	s_cbranch_vccnz .LBB0_889
	s_mov_b64 s[22:23], 0
	s_mov_b64 s[16:17], -1

; __device__ __forceinline__ unsigned xb_ld(unsigned* p)              { return __hip_atomic_load(p, __ATOMIC_RELAXED, __HIP_MEMORY_SCOPE_AGENT); }
; __device__ __forceinline__ void xcd_barrier_complete(unsigned* bar, unsigned x, unsigned& nloc, unsigned& nx, unsigned& bal) {
;     ...
;     for (;;) {
;         sum = 0u; cnt = 0u; mine = 0u; even = 1u;
; #pragma unroll
;         for (unsigned j = 0; j < 16; ++j) { const unsigned c = xb_ld(&bar[XB_XCNT(j)]); sum += c; cnt += (c > 0u) ? 1u : 0u; mine = (j == x) ? c : mine; even &= (c == (j < 8u ? G / 8u : 0u)) ? 1u : 0u; }
;         if (sum == G) break;
;         __builtin_amdgcn_s_sleep(1);
;         if ((++sp & 255u) == 0u) { if (xb_ld(&bar[XB_TMO])) break; if (sp > XB_SPIN_CAP) { atomicAdd(&bar[XB_TMO], 1u); break; } }
;     }
.LBB0_903:
	global_load_dword v9, v8, s[28:29] offset:1024 sc1
	global_load_dword v10, v8, s[28:29] offset:1280 sc1
	global_load_dword v11, v8, s[28:29] offset:1536 sc1
	global_load_dword v12, v8, s[28:29] offset:1792 sc1
	global_load_dword v13, v8, s[28:29] offset:2048 sc1
	global_load_dword v14, v8, s[28:29] offset:2304 sc1
	global_load_dword v15, v8, s[28:29] offset:2560 sc1
	global_load_dword v16, v8, s[28:29] offset:2816 sc1
	global_load_dword v0, v8, s[28:29] offset:3072 sc1
	global_load_dword v1, v8, s[28:29] offset:3328 sc1
	global_load_dword v2, v8, s[28:29] offset:3584 sc1
	global_load_dword v3, v8, s[28:29] offset:3840 sc1
	global_load_dword v4, v8, s[6:7] sc1
	global_load_dword v5, v8, s[8:9] sc1
	global_load_dword v6, v8, s[10:11] sc1
	global_load_dword v7, v8, s[12:13] sc1
	s_waitcnt vmcnt(15)
	v_readfirstlane_b32 s40, v9
	s_waitcnt vmcnt(14)
	v_add_u32_e32 v9, v10, v9
	s_waitcnt vmcnt(13)
	v_add_u32_e32 v9, v9, v11
	s_waitcnt vmcnt(12)
	v_add_u32_e32 v9, v9, v12
	s_waitcnt vmcnt(11)
	v_add_u32_e32 v9, v9, v13
	s_waitcnt vmcnt(10)
	v_add_u32_e32 v9, v9, v14
	s_waitcnt vmcnt(9)
	v_add_u32_e32 v9, v9, v15
	s_waitcnt vmcnt(8)
	v_add_u32_e32 v9, v9, v16
	s_waitcnt vmcnt(7)
	v_add_u32_e32 v9, v9, v0
	s_waitcnt vmcnt(6)
	v_add_u32_e32 v9, v9, v1
	s_waitcnt vmcnt(5)
	v_add_u32_e32 v9, v9, v2
	s_waitcnt vmcnt(4)
	v_add_u32_e32 v9, v9, v3
	s_waitcnt vmcnt(3)
	v_add_u32_e32 v9, v9, v4
	s_waitcnt vmcnt(2)
	v_add_u32_e32 v9, v9, v5
	s_waitcnt vmcnt(1)
	v_add_u32_e32 v9, v9, v6
	s_waitcnt vmcnt(0)
	v_add_u32_e32 v9, v9, v7
	v_cmp_eq_u32_e32 vcc, s3, v9
	v_readfirstlane_b32 s31, v10
	v_readfirstlane_b32 s36, v11
	v_readfirstlane_b32 s30, v12
	v_readfirstlane_b32 s27, v13
	v_readfirstlane_b32 s26, v14
	v_readfirstlane_b32 s37, v15
	v_readfirstlane_b32 s41, v16
	s_cbranch_vccnz .LBB0_901
	s_and_b32 s16, s42, 0xff
	s_mov_b64 s[22:23], -1
	s_mov_b64 s[14:15], 0
	s_cmp_eq_u32 s16, 0
	s_mov_b64 s[16:17], -1
	s_mov_b64 s[24:25], -1
	s_sleep 6
	s_cbranch_scc0 .LBB0_907
	global_load_dword v9, v8, s[28:29] offset:512 sc1
	s_mov_b64 s[16:17], 0
	s_mov_b64 s[14:15], -1
	s_mov_b64 s[24:25], 0
	s_waitcnt vmcnt(0)
	v_cmp_eq_u32_e32 vcc, 0, v9
	s_cbranch_vccz .LBB0_907
	s_cmp_lt_u32 s42, 0x40001
	s_mov_b64 s[14:15], 0
	s_cselect_b64 s[24:25], -1, 0

; __device__ __forceinline__ unsigned xb_ld(unsigned* p)              { return __hip_atomic_load(p, __ATOMIC_RELAXED, __HIP_MEMORY_SCOPE_AGENT); }
; __device__ __forceinline__ unsigned xb_add(unsigned* p, unsigned v) { return __hip_atomic_fetch_add(p, v, __ATOMIC_RELAXED, __HIP_MEMORY_SCOPE_AGENT); }
; #define XB_SPIN(cond, bar) do { unsigned _sp = 0; while (cond) { __builtin_amdgcn_s_sleep(1); \
;     if ((++_sp & 255u) == 0u) { if (xb_ld(&(bar)[XB_TMO])) break; if (_sp > XB_SPIN_CAP) { atomicAdd(&(bar)[XB_TMO], 1u); break; } } } } while (0)
; __device__ __forceinline__ void xcd_barrier(const XcdBarrier& b, const bool xb_leader) {
;     ...
;             const unsigned og = xb_add(&bar[XB_TOP], 1u);
;             const unsigned tg = og / nx;
;             if (og + 1u == (tg + 1u) * nx) xb_add(&bar[XB_TOPGEN], 1u);
;             else XB_SPIN(xb_ld(&bar[XB_TOPGEN]) == tg, bar);
.LBB0_928:
	s_and_b32 s24, s3, 0xff
	s_mov_b64 s[22:23], -1
	s_cmp_lg_u32 s24, 0
	s_mov_b64 s[26:27], -1
	s_sleep 6
	s_cbranch_scc1 .LBB0_931
	global_load_dword v2, v1, s[28:29] offset:512 sc1
	s_waitcnt vmcnt(0)
	v_cmp_eq_u32_e32 vcc, 0, v2
	s_cbranch_vccnz .LBB0_933
	s_mov_b64 s[26:27], 0
	s_mov_b64 s[24:25], -1

; __device__ __forceinline__ unsigned xb_ld(unsigned* p)              { return __hip_atomic_load(p, __ATOMIC_RELAXED, __HIP_MEMORY_SCOPE_AGENT); }
; #define XB_SPIN(cond, bar) do { unsigned _sp = 0; while (cond) { __builtin_amdgcn_s_sleep(1); \
;     if ((++_sp & 255u) == 0u) { if (xb_ld(&(bar)[XB_TMO])) break; if (_sp > XB_SPIN_CAP) { atomicAdd(&(bar)[XB_TMO], 1u); break; } } } } while (0)
; __device__ __forceinline__ void xcd_barrier(const XcdBarrier& b, const bool xb_leader) {
;     ...
;         } else {
;             XB_SPIN(xb_ld(&bar[XB_XGEN(b.x)]) == gen, bar);
;             __builtin_amdgcn_fence(__ATOMIC_ACQUIRE, "agent");
.LBB0_945:
	s_and_b32 s24, s3, 0xff
	s_cmp_lg_u32 s24, 0
	s_mov_b64 s[26:27], -1
	s_sleep 6
	s_cbranch_scc1 .LBB0_948
	global_load_dword v1, v0, s[12:13] sc1
	s_waitcnt vmcnt(0)
	v_cmp_eq_u32_e32 vcc, 0, v1
	s_cbranch_vccnz .LBB0_950
	s_mov_b64 s[26:27], 0
	s_mov_b64 s[24:25], -1

; __device__ __forceinline__ unsigned xb_ld(unsigned* p)              { return __hip_atomic_load(p, __ATOMIC_RELAXED, __HIP_MEMORY_SCOPE_AGENT); }
; __device__ __forceinline__ void xcd_barrier_complete(unsigned* bar, unsigned x, unsigned& nloc, unsigned& nx, unsigned& bal) {
;     ...
;     for (;;) {
;         sum = 0u; cnt = 0u; mine = 0u; even = 1u;
; #pragma unroll
;         for (unsigned j = 0; j < 16; ++j) { const unsigned c = xb_ld(&bar[XB_XCNT(j)]); sum += c; cnt += (c > 0u) ? 1u : 0u; mine = (j == x) ? c : mine; even &= (c == (j < 8u ? G / 8u : 0u)) ? 1u : 0u; }
;         if (sum == G) break;
;         __builtin_amdgcn_s_sleep(1);
;         if ((++sp & 255u) == 0u) { if (xb_ld(&bar[XB_TMO])) break; if (sp > XB_SPIN_CAP) { atomicAdd(&bar[XB_TMO], 1u); break; } }
;     }
.LBB0_1053:
	global_load_dword v9, v8, s[28:29] offset:1024 sc1
	global_load_dword v10, v8, s[28:29] offset:1280 sc1
	global_load_dword v11, v8, s[28:29] offset:1536 sc1
	global_load_dword v12, v8, s[28:29] offset:1792 sc1
	global_load_dword v13, v8, s[28:29] offset:2048 sc1
	global_load_dword v14, v8, s[28:29] offset:2304 sc1
	global_load_dword v15, v8, s[28:29] offset:2560 sc1
	global_load_dword v16, v8, s[28:29] offset:2816 sc1
	global_load_dword v0, v8, s[28:29] offset:3072 sc1
	global_load_dword v1, v8, s[28:29] offset:3328 sc1
	global_load_dword v2, v8, s[28:29] offset:3584 sc1
	global_load_dword v3, v8, s[28:29] offset:3840 sc1
	global_load_dword v4, v8, s[4:5] sc1
	global_load_dword v5, v8, s[6:7] sc1
	global_load_dword v6, v8, s[8:9] sc1
	global_load_dword v7, v8, s[10:11] sc1
	s_waitcnt vmcnt(15)
	v_readfirstlane_b32 s40, v9
	s_waitcnt vmcnt(14)
	v_add_u32_e32 v9, v10, v9
	s_waitcnt vmcnt(13)
	v_add_u32_e32 v9, v9, v11
	s_waitcnt vmcnt(12)
	v_add_u32_e32 v9, v9, v12
	s_waitcnt vmcnt(11)
	v_add_u32_e32 v9, v9, v13
	s_waitcnt vmcnt(10)
	v_add_u32_e32 v9, v9, v14
	s_waitcnt vmcnt(9)
	v_add_u32_e32 v9, v9, v15
	s_waitcnt vmcnt(8)
	v_add_u32_e32 v9, v9, v16
	s_waitcnt vmcnt(7)
	v_add_u32_e32 v9, v9, v0
	s_waitcnt vmcnt(6)
	v_add_u32_e32 v9, v9, v1
	s_waitcnt vmcnt(5)
	v_add_u32_e32 v9, v9, v2
	s_waitcnt vmcnt(4)
	v_add_u32_e32 v9, v9, v3
	s_waitcnt vmcnt(3)
	v_add_u32_e32 v9, v9, v4
	s_waitcnt vmcnt(2)
	v_add_u32_e32 v9, v9, v5
	s_waitcnt vmcnt(1)
	v_add_u32_e32 v9, v9, v6
	s_waitcnt vmcnt(0)
	v_add_u32_e32 v9, v9, v7
	v_cmp_eq_u32_e32 vcc, s3, v9
	v_readfirstlane_b32 s31, v10
	v_readfirstlane_b32 s36, v11
	v_readfirstlane_b32 s30, v12
	v_readfirstlane_b32 s27, v13
	v_readfirstlane_b32 s26, v14
	v_readfirstlane_b32 s37, v15
	v_readfirstlane_b32 s41, v16
	s_cbranch_vccnz .LBB0_1051
	s_and_b32 s14, s42, 0xff
	s_mov_b64 s[16:17], -1
	s_mov_b64 s[12:13], 0
	s_cmp_eq_u32 s14, 0
	s_mov_b64 s[14:15], -1
	s_mov_b64 s[24:25], -1
	s_sleep 6
	s_cbranch_scc0 .LBB0_1057
	global_load_dword v9, v8, s[28:29] offset:512 sc1
	s_mov_b64 s[14:15], 0
	s_mov_b64 s[12:13], -1
	s_mov_b64 s[24:25], 0
	s_waitcnt vmcnt(0)
	v_cmp_eq_u32_e32 vcc, 0, v9
	s_cbranch_vccz .LBB0_1057
	s_cmp_lt_u32 s42, 0x40001
	s_mov_b64 s[12:13], 0
	s_cselect_b64 s[24:25], -1, 0

; __device__ __forceinline__ unsigned xb_ld(unsigned* p)              { return __hip_atomic_load(p, __ATOMIC_RELAXED, __HIP_MEMORY_SCOPE_AGENT); }
; __device__ __forceinline__ unsigned xb_add(unsigned* p, unsigned v) { return __hip_atomic_fetch_add(p, v, __ATOMIC_RELAXED, __HIP_MEMORY_SCOPE_AGENT); }
; #define XB_SPIN(cond, bar) do { unsigned _sp = 0; while (cond) { __builtin_amdgcn_s_sleep(1); \
;     if ((++_sp & 255u) == 0u) { if (xb_ld(&(bar)[XB_TMO])) break; if (_sp > XB_SPIN_CAP) { atomicAdd(&(bar)[XB_TMO], 1u); break; } } } } while (0)
; __device__ __forceinline__ void xcd_barrier(const XcdBarrier& b, const bool xb_leader) {
;     ...
;             const unsigned og = xb_add(&bar[XB_TOP], 1u);
;             const unsigned tg = og / nx;
;             if (og + 1u == (tg + 1u) * nx) xb_add(&bar[XB_TOPGEN], 1u);
;             else XB_SPIN(xb_ld(&bar[XB_TOPGEN]) == tg, bar);
.LBB0_1078:
	s_and_b32 s24, s3, 0xff
	s_mov_b64 s[16:17], -1
	s_cmp_lg_u32 s24, 0
	s_mov_b64 s[26:27], -1
	s_sleep 6
	s_cbranch_scc1 .LBB0_1081
	global_load_dword v2, v1, s[28:29] offset:512 sc1
	s_waitcnt vmcnt(0)
	v_cmp_eq_u32_e32 vcc, 0, v2
	s_cbranch_vccnz .LBB0_1083
	s_mov_b64 s[26:27], 0
	s_mov_b64 s[24:25], -1

; __device__ __forceinline__ unsigned xb_ld(unsigned* p)              { return __hip_atomic_load(p, __ATOMIC_RELAXED, __HIP_MEMORY_SCOPE_AGENT); }
; #define XB_SPIN(cond, bar) do { unsigned _sp = 0; while (cond) { __builtin_amdgcn_s_sleep(1); \
;     if ((++_sp & 255u) == 0u) { if (xb_ld(&(bar)[XB_TMO])) break; if (_sp > XB_SPIN_CAP) { atomicAdd(&(bar)[XB_TMO], 1u); break; } } } } while (0)
; __device__ __forceinline__ void xcd_barrier(const XcdBarrier& b, const bool xb_leader) {
;     ...
;         } else {
;             XB_SPIN(xb_ld(&bar[XB_XGEN(b.x)]) == gen, bar);
;             __builtin_amdgcn_fence(__ATOMIC_ACQUIRE, "agent");
.LBB0_1095:
	s_and_b32 s24, s3, 0xff
	s_cmp_lg_u32 s24, 0
	s_mov_b64 s[26:27], -1
	s_sleep 6
	s_cbranch_scc1 .LBB0_1098
	global_load_dword v1, v0, s[10:11] sc1
	s_waitcnt vmcnt(0)
	v_cmp_eq_u32_e32 vcc, 0, v1
	s_cbranch_vccnz .LBB0_1100
	s_mov_b64 s[26:27], 0
	s_mov_b64 s[24:25], -1

; __device__ __forceinline__ unsigned xb_ld(unsigned* p)              { return __hip_atomic_load(p, __ATOMIC_RELAXED, __HIP_MEMORY_SCOPE_AGENT); }
; __device__ __forceinline__ void xcd_barrier_complete(unsigned* bar, unsigned x, unsigned& nloc, unsigned& nx, unsigned& bal) {
;     ...
;     for (;;) {
;         sum = 0u; cnt = 0u; mine = 0u; even = 1u;
; #pragma unroll
;         for (unsigned j = 0; j < 16; ++j) { const unsigned c = xb_ld(&bar[XB_XCNT(j)]); sum += c; cnt += (c > 0u) ? 1u : 0u; mine = (j == x) ? c : mine; even &= (c == (j < 8u ? G / 8u : 0u)) ? 1u : 0u; }
;         if (sum == G) break;
;         __builtin_amdgcn_s_sleep(1);
;         if ((++sp & 255u) == 0u) { if (xb_ld(&bar[XB_TMO])) break; if (sp > XB_SPIN_CAP) { atomicAdd(&bar[XB_TMO], 1u); break; } }
;     }
.LBB0_1193:
	global_load_dword v9, v8, s[28:29] offset:1024 sc1
	global_load_dword v10, v8, s[28:29] offset:1280 sc1
	global_load_dword v11, v8, s[28:29] offset:1536 sc1
	global_load_dword v12, v8, s[28:29] offset:1792 sc1
	global_load_dword v13, v8, s[28:29] offset:2048 sc1
	global_load_dword v14, v8, s[28:29] offset:2304 sc1
	global_load_dword v15, v8, s[28:29] offset:2560 sc1
	global_load_dword v16, v8, s[28:29] offset:2816 sc1
	global_load_dword v0, v8, s[28:29] offset:3072 sc1
	global_load_dword v1, v8, s[28:29] offset:3328 sc1
	global_load_dword v2, v8, s[28:29] offset:3584 sc1
	global_load_dword v3, v8, s[28:29] offset:3840 sc1
	global_load_dword v4, v8, s[6:7] sc1
	global_load_dword v5, v8, s[8:9] sc1
	global_load_dword v6, v8, s[10:11] sc1
	global_load_dword v7, v8, s[12:13] sc1
	s_waitcnt vmcnt(15)
	v_readfirstlane_b32 s42, v9
	s_waitcnt vmcnt(14)
	v_add_u32_e32 v9, v10, v9
	s_waitcnt vmcnt(13)
	v_add_u32_e32 v9, v9, v11
	s_waitcnt vmcnt(12)
	v_add_u32_e32 v9, v9, v12
	s_waitcnt vmcnt(11)
	v_add_u32_e32 v9, v9, v13
	s_waitcnt vmcnt(10)
	v_add_u32_e32 v9, v9, v14
	s_waitcnt vmcnt(9)
	v_add_u32_e32 v9, v9, v15
	s_waitcnt vmcnt(8)
	v_add_u32_e32 v9, v9, v16
	s_waitcnt vmcnt(7)
	v_add_u32_e32 v9, v9, v0
	s_waitcnt vmcnt(6)
	v_add_u32_e32 v9, v9, v1
	s_waitcnt vmcnt(5)
	v_add_u32_e32 v9, v9, v2
	s_waitcnt vmcnt(4)
	v_add_u32_e32 v9, v9, v3
	s_waitcnt vmcnt(3)
	v_add_u32_e32 v9, v9, v4
	s_waitcnt vmcnt(2)
	v_add_u32_e32 v9, v9, v5
	s_waitcnt vmcnt(1)
	v_add_u32_e32 v9, v9, v6
	s_waitcnt vmcnt(0)
	v_add_u32_e32 v9, v9, v7
	v_cmp_eq_u32_e32 vcc, s3, v9
	v_readfirstlane_b32 s37, v10
	v_readfirstlane_b32 s40, v11
	v_readfirstlane_b32 s36, v12
	v_readfirstlane_b32 s31, v13
	v_readfirstlane_b32 s30, v14
	v_readfirstlane_b32 s41, v15
	v_readfirstlane_b32 s43, v16
	s_cbranch_vccnz .LBB0_1191
	s_and_b32 s16, s44, 0xff
	s_mov_b64 s[24:25], -1
	s_mov_b64 s[14:15], 0
	s_cmp_eq_u32 s16, 0
	s_mov_b64 s[16:17], -1
	s_mov_b64 s[26:27], -1
	s_sleep 6
	s_cbranch_scc0 .LBB0_1196
	global_load_dword v9, v8, s[28:29] offset:512 sc1
	s_mov_b64 s[16:17], 0
	s_mov_b64 s[14:15], -1
	s_mov_b64 s[26:27], 0
	s_waitcnt vmcnt(0)
	v_cmp_eq_u32_e32 vcc, 0, v9
	s_cbranch_vccnz .LBB0_1198

; __device__ __forceinline__ unsigned xb_ld(unsigned* p)              { return __hip_atomic_load(p, __ATOMIC_RELAXED, __HIP_MEMORY_SCOPE_AGENT); }
; __device__ __forceinline__ unsigned xb_add(unsigned* p, unsigned v) { return __hip_atomic_fetch_add(p, v, __ATOMIC_RELAXED, __HIP_MEMORY_SCOPE_AGENT); }
; #define XB_SPIN(cond, bar) do { unsigned _sp = 0; while (cond) { __builtin_amdgcn_s_sleep(1); \
;     if ((++_sp & 255u) == 0u) { if (xb_ld(&(bar)[XB_TMO])) break; if (_sp > XB_SPIN_CAP) { atomicAdd(&(bar)[XB_TMO], 1u); break; } } } } while (0)
; __device__ __forceinline__ void xcd_barrier(const XcdBarrier& b, const bool xb_leader) {
;     ...
;             const unsigned og = xb_add(&bar[XB_TOP], 1u);
;             const unsigned tg = og / nx;
;             if (og + 1u == (tg + 1u) * nx) xb_add(&bar[XB_TOPGEN], 1u);
;             else XB_SPIN(xb_ld(&bar[XB_TOPGEN]) == tg, bar);
.LBB0_1217:
	s_and_b32 s26, s3, 0xff
	s_mov_b64 s[24:25], -1
	s_cmp_lg_u32 s26, 0
	s_mov_b64 s[30:31], -1
	s_sleep 6
	s_cbranch_scc1 .LBB0_1220
	global_load_dword v2, v1, s[28:29] offset:512 sc1
	s_waitcnt vmcnt(0)
	v_cmp_eq_u32_e32 vcc, 0, v2
	s_cbranch_vccnz .LBB0_1222
	s_mov_b64 s[30:31], 0
	s_mov_b64 s[26:27], -1

; __device__ __forceinline__ unsigned xb_ld(unsigned* p)              { return __hip_atomic_load(p, __ATOMIC_RELAXED, __HIP_MEMORY_SCOPE_AGENT); }
; #define XB_SPIN(cond, bar) do { unsigned _sp = 0; while (cond) { __builtin_amdgcn_s_sleep(1); \
;     if ((++_sp & 255u) == 0u) { if (xb_ld(&(bar)[XB_TMO])) break; if (_sp > XB_SPIN_CAP) { atomicAdd(&(bar)[XB_TMO], 1u); break; } } } } while (0)
; __device__ __forceinline__ void xcd_barrier(const XcdBarrier& b, const bool xb_leader) {
;     ...
;         } else {
;             XB_SPIN(xb_ld(&bar[XB_XGEN(b.x)]) == gen, bar);
;             __builtin_amdgcn_fence(__ATOMIC_ACQUIRE, "agent");
.LBB0_1234:
	s_and_b32 s26, s3, 0xff
	s_cmp_lg_u32 s26, 0
	s_mov_b64 s[30:31], -1
	s_sleep 6
	s_cbranch_scc1 .LBB0_1237
	global_load_dword v1, v0, s[12:13] sc1
	s_waitcnt vmcnt(0)
	v_cmp_eq_u32_e32 vcc, 0, v1
	s_cbranch_vccnz .LBB0_1239
	s_mov_b64 s[30:31], 0
	s_mov_b64 s[26:27], -1

; __device__ __forceinline__ unsigned xb_ld(unsigned* p)              { return __hip_atomic_load(p, __ATOMIC_RELAXED, __HIP_MEMORY_SCOPE_AGENT); }
; __device__ __forceinline__ unsigned xb_add(unsigned* p, unsigned v) { return __hip_atomic_fetch_add(p, v, __ATOMIC_RELAXED, __HIP_MEMORY_SCOPE_AGENT); }
; #define XB_SPIN(cond, bar) do { unsigned _sp = 0; while (cond) { __builtin_amdgcn_s_sleep(1); \
;     if ((++_sp & 255u) == 0u) { if (xb_ld(&(bar)[XB_TMO])) break; if (_sp > XB_SPIN_CAP) { atomicAdd(&(bar)[XB_TMO], 1u); break; } } } } while (0)
; __device__ __forceinline__ void xcc_barrier(unsigned* bar, unsigned* cnt, unsigned nloc, const bool xb_leader) {
;     ...
;     if (xb_leader) {
;         __builtin_amdgcn_s_waitcnt(0);
;         const unsigned old = xb_add(cnt, 1u), target = (old / nloc + 1u) * nloc;
;         XB_SPIN(xb_ld(cnt) < target, bar);
.LBB0_1445:
	s_and_b32 s16, s3, 0xff
	s_mov_b64 s[14:15], -1
	s_cmp_lg_u32 s16, 0
	s_mov_b64 s[24:25], -1
	s_sleep 6
	s_cbranch_scc1 .LBB0_1448
	global_load_dword v2, v0, s[28:29] offset:512 sc1
	s_waitcnt vmcnt(0)
	v_cmp_eq_u32_e32 vcc, 0, v2
	s_cbranch_vccnz .LBB0_1450
	s_mov_b64 s[24:25], 0
	s_mov_b64 s[16:17], -1

; __device__ __forceinline__ unsigned xb_ld(unsigned* p)              { return __hip_atomic_load(p, __ATOMIC_RELAXED, __HIP_MEMORY_SCOPE_AGENT); }
; __device__ __forceinline__ void xcd_barrier_complete(unsigned* bar, unsigned x, unsigned& nloc, unsigned& nx, unsigned& bal) {
;     ...
;     for (;;) {
;         sum = 0u; cnt = 0u; mine = 0u; even = 1u;
; #pragma unroll
;         for (unsigned j = 0; j < 16; ++j) { const unsigned c = xb_ld(&bar[XB_XCNT(j)]); sum += c; cnt += (c > 0u) ? 1u : 0u; mine = (j == x) ? c : mine; even &= (c == (j < 8u ? G / 8u : 0u)) ? 1u : 0u; }
;         if (sum == G) break;
;         __builtin_amdgcn_s_sleep(1);
;         if ((++sp & 255u) == 0u) { if (xb_ld(&bar[XB_TMO])) break; if (sp > XB_SPIN_CAP) { atomicAdd(&bar[XB_TMO], 1u); break; } }
;     }
.LBB0_1464:
	global_load_dword v9, v8, s[28:29] offset:1024 sc1
	global_load_dword v10, v8, s[28:29] offset:1280 sc1
	global_load_dword v11, v8, s[28:29] offset:1536 sc1
	global_load_dword v12, v8, s[28:29] offset:1792 sc1
	global_load_dword v13, v8, s[28:29] offset:2048 sc1
	global_load_dword v14, v8, s[28:29] offset:2304 sc1
	global_load_dword v15, v8, s[28:29] offset:2560 sc1
	global_load_dword v16, v8, s[28:29] offset:2816 sc1
	global_load_dword v0, v8, s[28:29] offset:3072 sc1
	global_load_dword v1, v8, s[28:29] offset:3328 sc1
	global_load_dword v2, v8, s[28:29] offset:3584 sc1
	global_load_dword v3, v8, s[28:29] offset:3840 sc1
	global_load_dword v4, v8, s[6:7] sc1
	global_load_dword v5, v8, s[8:9] sc1
	global_load_dword v6, v8, s[10:11] sc1
	global_load_dword v7, v8, s[12:13] sc1
	s_waitcnt vmcnt(15)
	v_readfirstlane_b32 s40, v9
	s_waitcnt vmcnt(14)
	v_add_u32_e32 v9, v10, v9
	s_waitcnt vmcnt(13)
	v_add_u32_e32 v9, v9, v11
	s_waitcnt vmcnt(12)
	v_add_u32_e32 v9, v9, v12
	s_waitcnt vmcnt(11)
	v_add_u32_e32 v9, v9, v13
	s_waitcnt vmcnt(10)
	v_add_u32_e32 v9, v9, v14
	s_waitcnt vmcnt(9)
	v_add_u32_e32 v9, v9, v15
	s_waitcnt vmcnt(8)
	v_add_u32_e32 v9, v9, v16
	s_waitcnt vmcnt(7)
	v_add_u32_e32 v9, v9, v0
	s_waitcnt vmcnt(6)
	v_add_u32_e32 v9, v9, v1
	s_waitcnt vmcnt(5)
	v_add_u32_e32 v9, v9, v2
	s_waitcnt vmcnt(4)
	v_add_u32_e32 v9, v9, v3
	s_waitcnt vmcnt(3)
	v_add_u32_e32 v9, v9, v4
	s_waitcnt vmcnt(2)
	v_add_u32_e32 v9, v9, v5
	s_waitcnt vmcnt(1)
	v_add_u32_e32 v9, v9, v6
	s_waitcnt vmcnt(0)
	v_add_u32_e32 v9, v9, v7
	v_cmp_eq_u32_e32 vcc, s3, v9
	v_readfirstlane_b32 s37, v10
	v_readfirstlane_b32 s38, v11
	v_readfirstlane_b32 s36, v12
	v_readfirstlane_b32 s31, v13
	v_readfirstlane_b32 s30, v14
	v_readfirstlane_b32 s39, v15
	v_readfirstlane_b32 s41, v16
	s_cbranch_vccnz .LBB0_1462
	s_and_b32 s16, s42, 0xff
	s_mov_b64 s[24:25], -1
	s_mov_b64 s[14:15], 0
	s_cmp_eq_u32 s16, 0
	s_mov_b64 s[16:17], -1
	s_mov_b64 s[26:27], -1
	s_sleep 6
	s_cbranch_scc0 .LBB0_1468
	global_load_dword v9, v8, s[28:29] offset:512 sc1
	s_mov_b64 s[16:17], 0
	s_mov_b64 s[14:15], -1
	s_mov_b64 s[26:27], 0
	s_waitcnt vmcnt(0)
	v_cmp_eq_u32_e32 vcc, 0, v9
	s_cbranch_vccz .LBB0_1468
	s_cmp_lt_u32 s42, 0x40001
	s_mov_b64 s[14:15], 0
	s_cselect_b64 s[26:27], -1, 0

; __device__ __forceinline__ unsigned xb_ld(unsigned* p)              { return __hip_atomic_load(p, __ATOMIC_RELAXED, __HIP_MEMORY_SCOPE_AGENT); }
; __device__ __forceinline__ void xcd_barrier_complete(unsigned* bar, unsigned x, unsigned& nloc, unsigned& nx, unsigned& bal) {
;     ...
;     for (;;) {
;         sum = 0u; cnt = 0u; mine = 0u; even = 1u;
; #pragma unroll
;         for (unsigned j = 0; j < 16; ++j) { const unsigned c = xb_ld(&bar[XB_XCNT(j)]); sum += c; cnt += (c > 0u) ? 1u : 0u; mine = (j == x) ? c : mine; even &= (c == (j < 8u ? G / 8u : 0u)) ? 1u : 0u; }
;         if (sum == G) break;
;         __builtin_amdgcn_s_sleep(1);
;         if ((++sp & 255u) == 0u) { if (xb_ld(&bar[XB_TMO])) break; if (sp > XB_SPIN_CAP) { atomicAdd(&bar[XB_TMO], 1u); break; } }
;     }
.LBB0_1571:
	global_load_dword v9, v8, s[28:29] offset:1024 sc1
	global_load_dword v10, v8, s[28:29] offset:1280 sc1
	global_load_dword v11, v8, s[28:29] offset:1536 sc1
	global_load_dword v12, v8, s[28:29] offset:1792 sc1
	global_load_dword v13, v8, s[28:29] offset:2048 sc1
	global_load_dword v14, v8, s[28:29] offset:2304 sc1
	global_load_dword v15, v8, s[28:29] offset:2560 sc1
	global_load_dword v16, v8, s[28:29] offset:2816 sc1
	global_load_dword v0, v8, s[28:29] offset:3072 sc1
	global_load_dword v1, v8, s[28:29] offset:3328 sc1
	global_load_dword v2, v8, s[28:29] offset:3584 sc1
	global_load_dword v3, v8, s[28:29] offset:3840 sc1
	global_load_dword v4, v8, s[4:5] sc1
	global_load_dword v5, v8, s[6:7] sc1
	global_load_dword v6, v8, s[10:11] sc1
	global_load_dword v7, v8, s[12:13] sc1
	s_waitcnt vmcnt(15)
	v_readfirstlane_b32 s38, v9
	s_waitcnt vmcnt(14)
	v_add_u32_e32 v9, v10, v9
	s_waitcnt vmcnt(13)
	v_add_u32_e32 v9, v9, v11
	s_waitcnt vmcnt(12)
	v_add_u32_e32 v9, v9, v12
	s_waitcnt vmcnt(11)
	v_add_u32_e32 v9, v9, v13
	s_waitcnt vmcnt(10)
	v_add_u32_e32 v9, v9, v14
	s_waitcnt vmcnt(9)
	v_add_u32_e32 v9, v9, v15
	s_waitcnt vmcnt(8)
	v_add_u32_e32 v9, v9, v16
	s_waitcnt vmcnt(7)
	v_add_u32_e32 v9, v9, v0
	s_waitcnt vmcnt(6)
	v_add_u32_e32 v9, v9, v1
	s_waitcnt vmcnt(5)
	v_add_u32_e32 v9, v9, v2
	s_waitcnt vmcnt(4)
	v_add_u32_e32 v9, v9, v3
	s_waitcnt vmcnt(3)
	v_add_u32_e32 v9, v9, v4
	s_waitcnt vmcnt(2)
	v_add_u32_e32 v9, v9, v5
	s_waitcnt vmcnt(1)
	v_add_u32_e32 v9, v9, v6
	s_waitcnt vmcnt(0)
	v_add_u32_e32 v9, v9, v7
	v_cmp_eq_u32_e32 vcc, s3, v9
	v_readfirstlane_b32 s31, v10
	v_readfirstlane_b32 s36, v11
	v_readfirstlane_b32 s30, v12
	v_readfirstlane_b32 s27, v13
	v_readfirstlane_b32 s26, v14
	v_readfirstlane_b32 s37, v15
	v_readfirstlane_b32 s39, v16
	s_cbranch_vccnz .LBB0_1569
	s_and_b32 s16, s40, 0xff
	s_mov_b64 s[22:23], -1
	s_mov_b64 s[14:15], 0
	s_cmp_eq_u32 s16, 0
	s_mov_b64 s[16:17], -1
	s_mov_b64 s[24:25], -1
	s_sleep 6
	s_cbranch_scc0 .LBB0_1575
	global_load_dword v9, v8, s[28:29] offset:512 sc1
	s_mov_b64 s[16:17], 0
	s_mov_b64 s[14:15], -1
	s_mov_b64 s[24:25], 0
	s_waitcnt vmcnt(0)
	v_cmp_eq_u32_e32 vcc, 0, v9
	s_cbranch_vccz .LBB0_1575
	s_cmp_lt_u32 s40, 0x40001
	s_mov_b64 s[14:15], 0
	s_cselect_b64 s[24:25], -1, 0

; __device__ __forceinline__ unsigned xb_ld(unsigned* p)              { return __hip_atomic_load(p, __ATOMIC_RELAXED, __HIP_MEMORY_SCOPE_AGENT); }
; __device__ __forceinline__ void xcd_barrier_complete(unsigned* bar, unsigned x, unsigned& nloc, unsigned& nx, unsigned& bal) {
;     ...
;     for (;;) {
;         sum = 0u; cnt = 0u; mine = 0u; even = 1u;
; #pragma unroll
;         for (unsigned j = 0; j < 16; ++j) { const unsigned c = xb_ld(&bar[XB_XCNT(j)]); sum += c; cnt += (c > 0u) ? 1u : 0u; mine = (j == x) ? c : mine; even &= (c == (j < 8u ? G / 8u : 0u)) ? 1u : 0u; }
;         if (sum == G) break;
;         __builtin_amdgcn_s_sleep(1);
;         if ((++sp & 255u) == 0u) { if (xb_ld(&bar[XB_TMO])) break; if (sp > XB_SPIN_CAP) { atomicAdd(&bar[XB_TMO], 1u); break; } }
;     }
.LBB0_1679:
	global_load_dword v9, v8, s[28:29] offset:1024 sc1
	global_load_dword v10, v8, s[28:29] offset:1280 sc1
	global_load_dword v11, v8, s[28:29] offset:1536 sc1
	global_load_dword v12, v8, s[28:29] offset:1792 sc1
	global_load_dword v13, v8, s[28:29] offset:2048 sc1
	global_load_dword v14, v8, s[28:29] offset:2304 sc1
	global_load_dword v15, v8, s[28:29] offset:2560 sc1
	global_load_dword v16, v8, s[28:29] offset:2816 sc1
	global_load_dword v0, v8, s[28:29] offset:3072 sc1
	global_load_dword v1, v8, s[28:29] offset:3328 sc1
	global_load_dword v2, v8, s[28:29] offset:3584 sc1
	global_load_dword v3, v8, s[28:29] offset:3840 sc1
	global_load_dword v4, v8, s[4:5] sc1
	global_load_dword v5, v8, s[6:7] sc1
	global_load_dword v6, v8, s[10:11] sc1
	global_load_dword v7, v8, s[12:13] sc1
	s_waitcnt vmcnt(15)
	v_readfirstlane_b32 s38, v9
	s_waitcnt vmcnt(14)
	v_add_u32_e32 v9, v10, v9
	s_waitcnt vmcnt(13)
	v_add_u32_e32 v9, v9, v11
	s_waitcnt vmcnt(12)
	v_add_u32_e32 v9, v9, v12
	s_waitcnt vmcnt(11)
	v_add_u32_e32 v9, v9, v13
	s_waitcnt vmcnt(10)
	v_add_u32_e32 v9, v9, v14
	s_waitcnt vmcnt(9)
	v_add_u32_e32 v9, v9, v15
	s_waitcnt vmcnt(8)
	v_add_u32_e32 v9, v9, v16
	s_waitcnt vmcnt(7)
	v_add_u32_e32 v9, v9, v0
	s_waitcnt vmcnt(6)
	v_add_u32_e32 v9, v9, v1
	s_waitcnt vmcnt(5)
	v_add_u32_e32 v9, v9, v2
	s_waitcnt vmcnt(4)
	v_add_u32_e32 v9, v9, v3
	s_waitcnt vmcnt(3)
	v_add_u32_e32 v9, v9, v4
	s_waitcnt vmcnt(2)
	v_add_u32_e32 v9, v9, v5
	s_waitcnt vmcnt(1)
	v_add_u32_e32 v9, v9, v6
	s_waitcnt vmcnt(0)
	v_add_u32_e32 v9, v9, v7
	v_cmp_eq_u32_e32 vcc, s3, v9
	v_readfirstlane_b32 s31, v10
	v_readfirstlane_b32 s36, v11
	v_readfirstlane_b32 s30, v12
	v_readfirstlane_b32 s27, v13
	v_readfirstlane_b32 s26, v14
	v_readfirstlane_b32 s37, v15
	v_readfirstlane_b32 s39, v16
	s_cbranch_vccnz .LBB0_1677
	s_and_b32 s16, s40, 0xff
	s_mov_b64 s[22:23], -1
	s_mov_b64 s[14:15], 0
	s_cmp_eq_u32 s16, 0
	s_mov_b64 s[16:17], -1
	s_mov_b64 s[24:25], -1
	s_sleep 6
	s_cbranch_scc0 .LBB0_1682
	global_load_dword v9, v8, s[28:29] offset:512 sc1
	s_mov_b64 s[16:17], 0
	s_mov_b64 s[14:15], -1
	s_mov_b64 s[24:25], 0
	s_waitcnt vmcnt(0)
	v_cmp_eq_u32_e32 vcc, 0, v9
	s_cbranch_vccnz .LBB0_1684

; __device__ __forceinline__ unsigned xb_ld(unsigned* p)              { return __hip_atomic_load(p, __ATOMIC_RELAXED, __HIP_MEMORY_SCOPE_AGENT); }
; __device__ __forceinline__ void xcd_barrier_complete(unsigned* bar, unsigned x, unsigned& nloc, unsigned& nx, unsigned& bal) {
;     ...
;     for (;;) {
;         sum = 0u; cnt = 0u; mine = 0u; even = 1u;
; #pragma unroll
;         for (unsigned j = 0; j < 16; ++j) { const unsigned c = xb_ld(&bar[XB_XCNT(j)]); sum += c; cnt += (c > 0u) ? 1u : 0u; mine = (j == x) ? c : mine; even &= (c == (j < 8u ? G / 8u : 0u)) ? 1u : 0u; }
;         if (sum == G) break;
;         __builtin_amdgcn_s_sleep(1);
;         if ((++sp & 255u) == 0u) { if (xb_ld(&bar[XB_TMO])) break; if (sp > XB_SPIN_CAP) { atomicAdd(&bar[XB_TMO], 1u); break; } }
;     }
.LBB0_1776:
	global_load_dword v9, v8, s[28:29] offset:1024 sc1
	global_load_dword v10, v8, s[28:29] offset:1280 sc1
	global_load_dword v11, v8, s[28:29] offset:1536 sc1
	global_load_dword v12, v8, s[28:29] offset:1792 sc1
	global_load_dword v13, v8, s[28:29] offset:2048 sc1
	global_load_dword v14, v8, s[28:29] offset:2304 sc1
	global_load_dword v15, v8, s[28:29] offset:2560 sc1
	global_load_dword v16, v8, s[28:29] offset:2816 sc1
	global_load_dword v0, v8, s[28:29] offset:3072 sc1
	global_load_dword v1, v8, s[28:29] offset:3328 sc1
	global_load_dword v2, v8, s[28:29] offset:3584 sc1
	global_load_dword v3, v8, s[28:29] offset:3840 sc1
	global_load_dword v4, v8, s[4:5] sc1
	global_load_dword v5, v8, s[6:7] sc1
	global_load_dword v6, v8, s[10:11] sc1
	global_load_dword v7, v8, s[12:13] sc1
	s_waitcnt vmcnt(15)
	v_readfirstlane_b32 s36, v9
	s_waitcnt vmcnt(14)
	v_add_u32_e32 v9, v10, v9
	s_waitcnt vmcnt(13)
	v_add_u32_e32 v9, v9, v11
	s_waitcnt vmcnt(12)
	v_add_u32_e32 v9, v9, v12
	s_waitcnt vmcnt(11)
	v_add_u32_e32 v9, v9, v13
	s_waitcnt vmcnt(10)
	v_add_u32_e32 v9, v9, v14
	s_waitcnt vmcnt(9)
	v_add_u32_e32 v9, v9, v15
	s_waitcnt vmcnt(8)
	v_add_u32_e32 v9, v9, v16
	s_waitcnt vmcnt(7)
	v_add_u32_e32 v9, v9, v0
	s_waitcnt vmcnt(6)
	v_add_u32_e32 v9, v9, v1
	s_waitcnt vmcnt(5)
	v_add_u32_e32 v9, v9, v2
	s_waitcnt vmcnt(4)
	v_add_u32_e32 v9, v9, v3
	s_waitcnt vmcnt(3)
	v_add_u32_e32 v9, v9, v4
	s_waitcnt vmcnt(2)
	v_add_u32_e32 v9, v9, v5
	s_waitcnt vmcnt(1)
	v_add_u32_e32 v9, v9, v6
	s_waitcnt vmcnt(0)
	v_add_u32_e32 v9, v9, v7
	v_cmp_eq_u32_e32 vcc, s3, v9
	v_readfirstlane_b32 s31, v10
	v_readfirstlane_b32 s34, v11
	v_readfirstlane_b32 s30, v12
	v_readfirstlane_b32 s27, v13
	v_readfirstlane_b32 s26, v14
	v_readfirstlane_b32 s35, v15
	v_readfirstlane_b32 s37, v16
	s_cbranch_vccnz .LBB0_1774
	s_and_b32 s16, s38, 0xff
	s_mov_b64 s[22:23], -1
	s_mov_b64 s[14:15], 0
	s_cmp_eq_u32 s16, 0
	s_mov_b64 s[16:17], -1
	s_mov_b64 s[24:25], -1
	s_sleep 6
	s_cbranch_scc0 .LBB0_1779
	global_load_dword v9, v8, s[28:29] offset:512 sc1
	s_mov_b64 s[16:17], 0
	s_mov_b64 s[14:15], -1
	s_mov_b64 s[24:25], 0
	s_waitcnt vmcnt(0)
	v_cmp_eq_u32_e32 vcc, 0, v9
	s_cbranch_vccnz .LBB0_1781

; __device__ __forceinline__ unsigned xb_ld(unsigned* p)              { return __hip_atomic_load(p, __ATOMIC_RELAXED, __HIP_MEMORY_SCOPE_AGENT); }
; __device__ __forceinline__ void xcd_barrier_complete(unsigned* bar, unsigned x, unsigned& nloc, unsigned& nx, unsigned& bal) {
;     ...
;     for (;;) {
;         sum = 0u; cnt = 0u; mine = 0u; even = 1u;
; #pragma unroll
;         for (unsigned j = 0; j < 16; ++j) { const unsigned c = xb_ld(&bar[XB_XCNT(j)]); sum += c; cnt += (c > 0u) ? 1u : 0u; mine = (j == x) ? c : mine; even &= (c == (j < 8u ? G / 8u : 0u)) ? 1u : 0u; }
;         if (sum == G) break;
;         __builtin_amdgcn_s_sleep(1);
;         if ((++sp & 255u) == 0u) { if (xb_ld(&bar[XB_TMO])) break; if (sp > XB_SPIN_CAP) { atomicAdd(&bar[XB_TMO], 1u); break; } }
;     }
.LBB0_1888:
	global_load_dword v9, v8, s[28:29] offset:1024 sc1
	global_load_dword v10, v8, s[28:29] offset:1280 sc1
	global_load_dword v11, v8, s[28:29] offset:1536 sc1
	global_load_dword v12, v8, s[28:29] offset:1792 sc1
	global_load_dword v13, v8, s[28:29] offset:2048 sc1
	global_load_dword v14, v8, s[28:29] offset:2304 sc1
	global_load_dword v15, v8, s[28:29] offset:2560 sc1
	global_load_dword v16, v8, s[28:29] offset:2816 sc1
	global_load_dword v0, v8, s[28:29] offset:3072 sc1
	global_load_dword v1, v8, s[28:29] offset:3328 sc1
	global_load_dword v2, v8, s[28:29] offset:3584 sc1
	global_load_dword v3, v8, s[28:29] offset:3840 sc1
	global_load_dword v4, v8, s[0:1] sc1
	global_load_dword v5, v8, s[2:3] sc1
	global_load_dword v6, v8, s[8:9] sc1
	global_load_dword v7, v8, s[12:13] sc1
	s_waitcnt vmcnt(15)
	v_readfirstlane_b32 s35, v9
	s_waitcnt vmcnt(14)
	v_add_u32_e32 v9, v10, v9
	s_waitcnt vmcnt(13)
	v_add_u32_e32 v9, v9, v11
	s_waitcnt vmcnt(12)
	v_add_u32_e32 v9, v9, v12
	s_waitcnt vmcnt(11)
	v_add_u32_e32 v9, v9, v13
	s_waitcnt vmcnt(10)
	v_add_u32_e32 v9, v9, v14
	s_waitcnt vmcnt(9)
	v_add_u32_e32 v9, v9, v15
	s_waitcnt vmcnt(8)
	v_add_u32_e32 v9, v9, v16
	s_waitcnt vmcnt(7)
	v_add_u32_e32 v9, v9, v0
	s_waitcnt vmcnt(6)
	v_add_u32_e32 v9, v9, v1
	s_waitcnt vmcnt(5)
	v_add_u32_e32 v9, v9, v2
	s_waitcnt vmcnt(4)
	v_add_u32_e32 v9, v9, v3
	s_waitcnt vmcnt(3)
	v_add_u32_e32 v9, v9, v4
	s_waitcnt vmcnt(2)
	v_add_u32_e32 v9, v9, v5
	s_waitcnt vmcnt(1)
	v_add_u32_e32 v9, v9, v6
	s_waitcnt vmcnt(0)
	v_add_u32_e32 v9, v9, v7
	v_cmp_eq_u32_e32 vcc, s24, v9
	v_readfirstlane_b32 s30, v10
	v_readfirstlane_b32 s31, v11
	v_readfirstlane_b32 s27, v12
	v_readfirstlane_b32 s26, v13
	v_readfirstlane_b32 s25, v14
	v_readfirstlane_b32 s34, v15
	v_readfirstlane_b32 s36, v16
	s_cbranch_vccnz .LBB0_1886
	s_and_b32 s16, s37, 0xff
	s_mov_b64 s[20:21], -1
	s_mov_b64 s[14:15], 0
	s_cmp_eq_u32 s16, 0
	s_mov_b64 s[16:17], -1
	s_mov_b64 s[22:23], -1
	s_sleep 6
	s_cbranch_scc0 .LBB0_1891
	global_load_dword v9, v8, s[28:29] offset:512 sc1
	s_mov_b64 s[16:17], 0
	s_mov_b64 s[14:15], -1
	s_mov_b64 s[22:23], 0
	s_waitcnt vmcnt(0)
	v_cmp_eq_u32_e32 vcc, 0, v9
	s_cbranch_vccnz .LBB0_1893

; __device__ __forceinline__ unsigned xb_ld(unsigned* p)              { return __hip_atomic_load(p, __ATOMIC_RELAXED, __HIP_MEMORY_SCOPE_AGENT); }
; __device__ __forceinline__ unsigned xb_add(unsigned* p, unsigned v) { return __hip_atomic_fetch_add(p, v, __ATOMIC_RELAXED, __HIP_MEMORY_SCOPE_AGENT); }
; #define XB_SPIN(cond, bar) do { unsigned _sp = 0; while (cond) { __builtin_amdgcn_s_sleep(1); \
;     if ((++_sp & 255u) == 0u) { if (xb_ld(&(bar)[XB_TMO])) break; if (_sp > XB_SPIN_CAP) { atomicAdd(&(bar)[XB_TMO], 1u); break; } } } } while (0)
; __device__ __forceinline__ void xcd_barrier(const XcdBarrier& b, const bool xb_leader) {
;     ...
;             const unsigned og = xb_add(&bar[XB_TOP], 1u);
;             const unsigned tg = og / nx;
;             if (og + 1u == (tg + 1u) * nx) xb_add(&bar[XB_TOPGEN], 1u);
;             else XB_SPIN(xb_ld(&bar[XB_TOPGEN]) == tg, bar);
.LBB0_1912:
	s_and_b32 s22, s26, 0xff
	s_mov_b64 s[20:21], -1
	s_cmp_lg_u32 s22, 0
	s_mov_b64 s[24:25], -1
	s_sleep 6
	s_cbranch_scc1 .LBB0_1915
	global_load_dword v2, v1, s[28:29] offset:512 sc1
	s_waitcnt vmcnt(0)
	v_cmp_eq_u32_e32 vcc, 0, v2
	s_cbranch_vccnz .LBB0_1917
	s_mov_b64 s[24:25], 0
	s_mov_b64 s[22:23], -1

; __device__ __forceinline__ unsigned xb_ld(unsigned* p)              { return __hip_atomic_load(p, __ATOMIC_RELAXED, __HIP_MEMORY_SCOPE_AGENT); }
; #define XB_SPIN(cond, bar) do { unsigned _sp = 0; while (cond) { __builtin_amdgcn_s_sleep(1); \
;     if ((++_sp & 255u) == 0u) { if (xb_ld(&(bar)[XB_TMO])) break; if (_sp > XB_SPIN_CAP) { atomicAdd(&(bar)[XB_TMO], 1u); break; } } } } while (0)
; __device__ __forceinline__ void xcd_barrier(const XcdBarrier& b, const bool xb_leader) {
;     ...
;         } else {
;             XB_SPIN(xb_ld(&bar[XB_XGEN(b.x)]) == gen, bar);
;             __builtin_amdgcn_fence(__ATOMIC_ACQUIRE, "agent");
.LBB0_1929:
	s_and_b32 s22, s28, 0xff
	s_cmp_lg_u32 s22, 0
	s_mov_b64 s[24:25], -1
	s_sleep 6
	s_cbranch_scc1 .LBB0_1932
	global_load_dword v1, v0, s[12:13] sc1
	s_waitcnt vmcnt(0)
	v_cmp_eq_u32_e32 vcc, 0, v1
	s_cbranch_vccnz .LBB0_1934
	s_mov_b64 s[24:25], 0
	s_mov_b64 s[22:23], -1
